# baseline (speedup 1.0000x reference)
.Lp1_loop:
	s_waitcnt vmcnt(0)
	ds_write_b128 v88, v[146:149]
	ds_write_b128 v89, v[150:153]
	ds_write_b128 v88, v[154:157] offset:9216
	ds_write_b128 v89, v[158:161] offset:9216
	global_load_dwordx4 v[112:115], v128, s[24:25]
	global_load_dwordx4 v[116:119], v86, s[24:25]
	s_add_u32 s24, s24, 0x2000
	s_addc_u32 s25, s25, 0
	global_load_dwordx4 v[120:123], v128, s[24:25]
	global_load_dwordx4 v[124:127], v86, s[24:25]
	s_add_u32 s24, s24, 0x2000
	s_addc_u32 s25, s25, 0
	ds_read_b128 v[168:171], v167
	ds_read_b128 v[172:175], v167 offset:4608
	ds_read_b128 v[176:179], v167 offset:32
	ds_read_b128 v[180:183], v167 offset:4640
	ds_read_b128 v[184:187], v167 offset:64
	ds_read_b128 v[188:191], v167 offset:4672
	ds_read_b128 v[192:195], v167 offset:96
	ds_read_b128 v[196:199], v167 offset:4704
	v_exp_f32_e32 v34, v34
	v_exp_f32_e32 v35, v35
	v_mov_b32_e32 v200, v34
	v_exp_f32_e32 v36, v36
	v_mov_b32_e32 v201, v35
	v_exp_f32_e32 v37, v37
	s_waitcnt lgkmcnt(7)
	v_mfma_f32_32x32x16_f16 v[2:17], v[168:171], v[108:111], v[130:145]
	v_mov_b32_e32 v202, v36
	v_exp_f32_e32 v38, v38
	v_mov_b32_e32 v83, v37
	v_exp_f32_e32 v39, v39
	v_add_f32_e32 v200, v200, v38
	v_exp_f32_e32 v40, v40
	s_waitcnt lgkmcnt(6)
	v_mfma_f32_32x32x16_f16 v[18:33], v[172:175], v[108:111], v[130:145]
	v_add_f32_e32 v201, v201, v39
	v_exp_f32_e32 v41, v41
	v_add_f32_e32 v202, v202, v40
	v_exp_f32_e32 v42, v42
	v_add_f32_e32 v83, v83, v41
	v_exp_f32_e32 v43, v43
	s_waitcnt lgkmcnt(5)
	v_mfma_f32_32x32x16_f16 v[2:17], v[176:179], v[104:107], v[2:17]
	v_add_f32_e32 v200, v200, v42
	v_exp_f32_e32 v44, v44
	v_add_f32_e32 v201, v201, v43
	v_exp_f32_e32 v45, v45
	v_add_f32_e32 v202, v202, v44
	v_exp_f32_e32 v46, v46
	s_waitcnt lgkmcnt(4)
	v_mfma_f32_32x32x16_f16 v[18:33], v[180:183], v[104:107], v[18:33]
	v_add_f32_e32 v83, v83, v45
	v_exp_f32_e32 v47, v47
	v_add_f32_e32 v200, v200, v46
	v_exp_f32_e32 v48, v48
	v_add_f32_e32 v201, v201, v47
	v_exp_f32_e32 v49, v49
	s_waitcnt lgkmcnt(3)
	v_mfma_f32_32x32x16_f16 v[2:17], v[184:187], v[100:103], v[2:17]
	v_add_f32_e32 v202, v202, v48
	v_exp_f32_e32 v50, v50
	v_add_f32_e32 v83, v83, v49
	v_exp_f32_e32 v51, v51
	v_add_f32_e32 v200, v200, v50
	v_exp_f32_e32 v52, v52
	s_waitcnt lgkmcnt(2)
	v_mfma_f32_32x32x16_f16 v[18:33], v[188:191], v[100:103], v[18:33]
	v_add_f32_e32 v201, v201, v51
	v_exp_f32_e32 v53, v53
	v_add_f32_e32 v202, v202, v52
	v_exp_f32_e32 v54, v54
	v_add_f32_e32 v83, v83, v53
	v_exp_f32_e32 v55, v55
	s_waitcnt lgkmcnt(1)
	v_mfma_f32_32x32x16_f16 v[2:17], v[192:195], v[96:99], v[2:17]
	v_add_f32_e32 v200, v200, v54
	v_exp_f32_e32 v56, v56
	v_add_f32_e32 v201, v201, v55
	v_exp_f32_e32 v57, v57
	v_add_f32_e32 v202, v202, v56
	v_exp_f32_e32 v58, v58
	s_waitcnt lgkmcnt(0)
	v_mfma_f32_32x32x16_f16 v[18:33], v[196:199], v[96:99], v[18:33]
	ds_read_b128 v[204:207], v167 offset:9216
	ds_read_b128 v[208:211], v167 offset:13824
	ds_read_b128 v[212:215], v167 offset:9248
	ds_read_b128 v[216:219], v167 offset:13856
	ds_read_b128 v[220:223], v167 offset:9280
	ds_read_b128 v[224:227], v167 offset:13888
	ds_read_b128 v[228:231], v167 offset:9312
	ds_read_b128 v[232:235], v167 offset:13920
	v_add_f32_e32 v83, v83, v57
	v_exp_f32_e32 v59, v59
	v_add_f32_e32 v200, v200, v58
	v_exp_f32_e32 v60, v60
	v_add_f32_e32 v201, v201, v59
	v_exp_f32_e32 v61, v61
	v_add_f32_e32 v202, v202, v60
	v_exp_f32_e32 v62, v62
	v_add_f32_e32 v83, v83, v61
	v_exp_f32_e32 v63, v63
	v_add_f32_e32 v200, v200, v62
	v_exp_f32_e32 v64, v64
	v_add_f32_e32 v201, v201, v63
	v_exp_f32_e32 v65, v65
	v_add_f32_e32 v202, v202, v64
	v_add_f32_e32 v83, v83, v65
	v_add_f32_e32 v200, v200, v201
	v_add_f32_e32 v202, v202, v83
	v_add_f32_e32 v200, v200, v202
	v_add_f32_e32 v82, v82, v200
	v_max3_f32 v84, v2, v3, v4
	v_max3_f32 v85, v18, v19, v20
	v_max3_f32 v84, v84, v5, v6
	v_max3_f32 v85, v85, v21, v22
	v_max3_f32 v84, v84, v7, v8
	v_max3_f32 v85, v85, v23, v24
	v_max3_f32 v84, v84, v9, v10
	v_max3_f32 v85, v85, v25, v26
	v_max3_f32 v84, v84, v11, v12
	v_max3_f32 v85, v85, v27, v28
	v_max3_f32 v84, v84, v13, v14
	v_max3_f32 v85, v85, v29, v30
	v_max3_f32 v84, v84, v15, v16
	v_max3_f32 v85, v85, v31, v32
	v_max3_f32 v84, v84, v17, v33
	v_max_f32_e32 v84, v84, v85
	v_cmp_lt_f32_e32 vcc, s11, v84
	s_cbranch_vccnz .Lp1_rare_d0a
.Lp1_back_d0a:
	v_exp_f32_e32 v2, v2
	v_exp_f32_e32 v3, v3
	v_mov_b32_e32 v200, v2
	v_exp_f32_e32 v4, v4
	v_mov_b32_e32 v201, v3
	v_exp_f32_e32 v5, v5
	s_waitcnt lgkmcnt(7)
	v_mfma_f32_32x32x16_f16 v[34:49], v[204:207], v[108:111], v[130:145]
	v_mov_b32_e32 v202, v4
	v_exp_f32_e32 v6, v6
	v_mov_b32_e32 v83, v5
	v_exp_f32_e32 v7, v7
	v_add_f32_e32 v200, v200, v6
	v_exp_f32_e32 v8, v8
	s_waitcnt lgkmcnt(6)
	v_mfma_f32_32x32x16_f16 v[50:65], v[208:211], v[108:111], v[130:145]
	v_add_f32_e32 v201, v201, v7
	v_exp_f32_e32 v9, v9
	v_add_f32_e32 v202, v202, v8
	v_exp_f32_e32 v10, v10
	v_add_f32_e32 v83, v83, v9
	v_exp_f32_e32 v11, v11
	s_waitcnt lgkmcnt(5)
	v_mfma_f32_32x32x16_f16 v[34:49], v[212:215], v[104:107], v[34:49]
	v_add_f32_e32 v200, v200, v10
	v_exp_f32_e32 v12, v12
	v_add_f32_e32 v201, v201, v11
	v_exp_f32_e32 v13, v13
	v_add_f32_e32 v202, v202, v12
	v_exp_f32_e32 v14, v14
	s_waitcnt lgkmcnt(4)
	v_mfma_f32_32x32x16_f16 v[50:65], v[216:219], v[104:107], v[50:65]
	v_add_f32_e32 v83, v83, v13
	v_exp_f32_e32 v15, v15
	v_add_f32_e32 v200, v200, v14
	v_exp_f32_e32 v16, v16
	v_add_f32_e32 v201, v201, v15
	v_exp_f32_e32 v17, v17
	s_waitcnt lgkmcnt(3)
	v_mfma_f32_32x32x16_f16 v[34:49], v[220:223], v[100:103], v[34:49]
	v_add_f32_e32 v202, v202, v16
	v_exp_f32_e32 v18, v18
	v_add_f32_e32 v83, v83, v17
	v_exp_f32_e32 v19, v19
	v_add_f32_e32 v200, v200, v18
	v_exp_f32_e32 v20, v20
	s_waitcnt lgkmcnt(2)
	v_mfma_f32_32x32x16_f16 v[50:65], v[224:227], v[100:103], v[50:65]
	v_add_f32_e32 v201, v201, v19
	v_exp_f32_e32 v21, v21
	v_add_f32_e32 v202, v202, v20
	v_exp_f32_e32 v22, v22
	v_add_f32_e32 v83, v83, v21
	v_exp_f32_e32 v23, v23
	s_waitcnt lgkmcnt(1)
	v_mfma_f32_32x32x16_f16 v[34:49], v[228:231], v[96:99], v[34:49]
	v_add_f32_e32 v200, v200, v22
	v_exp_f32_e32 v24, v24
	v_add_f32_e32 v201, v201, v23
	v_exp_f32_e32 v25, v25
	v_add_f32_e32 v202, v202, v24
	v_exp_f32_e32 v26, v26
	s_waitcnt lgkmcnt(0)
	v_mfma_f32_32x32x16_f16 v[50:65], v[232:235], v[96:99], v[50:65]
	v_add_f32_e32 v83, v83, v25
	v_exp_f32_e32 v27, v27
	v_add_f32_e32 v200, v200, v26
	v_exp_f32_e32 v28, v28
	v_add_f32_e32 v201, v201, v27
	v_exp_f32_e32 v29, v29
	v_add_f32_e32 v202, v202, v28
	v_exp_f32_e32 v30, v30
	v_add_f32_e32 v83, v83, v29
	v_exp_f32_e32 v31, v31
	v_add_f32_e32 v200, v200, v30
	v_exp_f32_e32 v32, v32
	v_add_f32_e32 v201, v201, v31
	v_exp_f32_e32 v33, v33
	v_add_f32_e32 v202, v202, v32
	v_add_f32_e32 v83, v83, v33
	v_add_f32_e32 v200, v200, v201
	v_add_f32_e32 v202, v202, v83
	v_add_f32_e32 v200, v200, v202
	v_add_f32_e32 v82, v82, v200
	v_max3_f32 v84, v34, v35, v36
	v_max3_f32 v85, v50, v51, v52
	v_max3_f32 v84, v84, v37, v38
	v_max3_f32 v85, v85, v53, v54
	v_max3_f32 v84, v84, v39, v40
	v_max3_f32 v85, v85, v55, v56
	v_max3_f32 v84, v84, v41, v42
	v_max3_f32 v85, v85, v57, v58
	v_max3_f32 v84, v84, v43, v44
	v_max3_f32 v85, v85, v59, v60
	v_max3_f32 v84, v84, v45, v46
	v_max3_f32 v85, v85, v61, v62
	v_max3_f32 v84, v84, v47, v48
	v_max3_f32 v85, v85, v63, v64
	v_max3_f32 v84, v84, v49, v65
	v_max_f32_e32 v84, v84, v85
	v_cmp_lt_f32_e32 vcc, s11, v84
	s_cbranch_vccnz .Lp1_rare_d0b
.Lp1_back_d0b:
	s_waitcnt lgkmcnt(0)
	s_barrier
	s_waitcnt vmcnt(0)
	ds_write_b128 v77, v[112:115]
	ds_write_b128 v78, v[116:119]
	ds_write_b128 v77, v[120:123] offset:9216
	ds_write_b128 v78, v[124:127] offset:9216
	global_load_dwordx4 v[146:149], v128, s[24:25]
	global_load_dwordx4 v[150:153], v86, s[24:25]
	s_add_u32 s24, s24, 0x2000
	s_addc_u32 s25, s25, 0
	global_load_dwordx4 v[154:157], v128, s[24:25]
	global_load_dwordx4 v[158:161], v86, s[24:25]
	s_add_u32 s24, s24, 0x2000
	s_addc_u32 s25, s25, 0
	ds_read_b128 v[168:171], v87
	ds_read_b128 v[172:175], v87 offset:4608
	ds_read_b128 v[176:179], v87 offset:32
	ds_read_b128 v[180:183], v87 offset:4640
	ds_read_b128 v[184:187], v87 offset:64
	ds_read_b128 v[188:191], v87 offset:4672
	ds_read_b128 v[192:195], v87 offset:96
	ds_read_b128 v[196:199], v87 offset:4704
	v_exp_f32_e32 v34, v34
	v_exp_f32_e32 v35, v35
	v_mov_b32_e32 v200, v34
	v_exp_f32_e32 v36, v36
	v_mov_b32_e32 v201, v35
	v_exp_f32_e32 v37, v37
	s_waitcnt lgkmcnt(7)
	v_mfma_f32_32x32x16_f16 v[2:17], v[168:171], v[108:111], v[130:145]
	v_mov_b32_e32 v202, v36
	v_exp_f32_e32 v38, v38
	v_mov_b32_e32 v83, v37
	v_exp_f32_e32 v39, v39
	v_add_f32_e32 v200, v200, v38
	v_exp_f32_e32 v40, v40
	s_waitcnt lgkmcnt(6)
	v_mfma_f32_32x32x16_f16 v[18:33], v[172:175], v[108:111], v[130:145]
	v_add_f32_e32 v201, v201, v39
	v_exp_f32_e32 v41, v41
	v_add_f32_e32 v202, v202, v40
	v_exp_f32_e32 v42, v42
	v_add_f32_e32 v83, v83, v41
	v_exp_f32_e32 v43, v43
	s_waitcnt lgkmcnt(5)
	v_mfma_f32_32x32x16_f16 v[2:17], v[176:179], v[104:107], v[2:17]
	v_add_f32_e32 v200, v200, v42
	v_exp_f32_e32 v44, v44
	v_add_f32_e32 v201, v201, v43
	v_exp_f32_e32 v45, v45
	v_add_f32_e32 v202, v202, v44
	v_exp_f32_e32 v46, v46
	s_waitcnt lgkmcnt(4)
	v_mfma_f32_32x32x16_f16 v[18:33], v[180:183], v[104:107], v[18:33]
	v_add_f32_e32 v83, v83, v45
	v_exp_f32_e32 v47, v47
	v_add_f32_e32 v200, v200, v46
	v_exp_f32_e32 v48, v48
	v_add_f32_e32 v201, v201, v47
	v_exp_f32_e32 v49, v49
	s_waitcnt lgkmcnt(3)
	v_mfma_f32_32x32x16_f16 v[2:17], v[184:187], v[100:103], v[2:17]
	v_add_f32_e32 v202, v202, v48
	v_exp_f32_e32 v50, v50
	v_add_f32_e32 v83, v83, v49
	v_exp_f32_e32 v51, v51
	v_add_f32_e32 v200, v200, v50
	v_exp_f32_e32 v52, v52
	s_waitcnt lgkmcnt(2)
	v_mfma_f32_32x32x16_f16 v[18:33], v[188:191], v[100:103], v[18:33]
	v_add_f32_e32 v201, v201, v51
	v_exp_f32_e32 v53, v53
	v_add_f32_e32 v202, v202, v52
	v_exp_f32_e32 v54, v54
	v_add_f32_e32 v83, v83, v53
	v_exp_f32_e32 v55, v55
	s_waitcnt lgkmcnt(1)
	v_mfma_f32_32x32x16_f16 v[2:17], v[192:195], v[96:99], v[2:17]
	v_add_f32_e32 v200, v200, v54
	v_exp_f32_e32 v56, v56
	v_add_f32_e32 v201, v201, v55
	v_exp_f32_e32 v57, v57
	v_add_f32_e32 v202, v202, v56
	v_exp_f32_e32 v58, v58
	s_waitcnt lgkmcnt(0)
	v_mfma_f32_32x32x16_f16 v[18:33], v[196:199], v[96:99], v[18:33]
	ds_read_b128 v[204:207], v87 offset:9216
	ds_read_b128 v[208:211], v87 offset:13824
	ds_read_b128 v[212:215], v87 offset:9248
	ds_read_b128 v[216:219], v87 offset:13856
	ds_read_b128 v[220:223], v87 offset:9280
	ds_read_b128 v[224:227], v87 offset:13888
	ds_read_b128 v[228:231], v87 offset:9312
	ds_read_b128 v[232:235], v87 offset:13920
	v_add_f32_e32 v83, v83, v57
	v_exp_f32_e32 v59, v59
	v_add_f32_e32 v200, v200, v58
	v_exp_f32_e32 v60, v60
	v_add_f32_e32 v201, v201, v59
	v_exp_f32_e32 v61, v61
	v_add_f32_e32 v202, v202, v60
	v_exp_f32_e32 v62, v62
	v_add_f32_e32 v83, v83, v61
	v_exp_f32_e32 v63, v63
	v_add_f32_e32 v200, v200, v62
	v_exp_f32_e32 v64, v64
	v_add_f32_e32 v201, v201, v63
	v_exp_f32_e32 v65, v65
	v_add_f32_e32 v202, v202, v64
	v_add_f32_e32 v83, v83, v65
	v_add_f32_e32 v200, v200, v201
	v_add_f32_e32 v202, v202, v83
	v_add_f32_e32 v200, v200, v202
	v_add_f32_e32 v82, v82, v200
	v_max3_f32 v84, v2, v3, v4
	v_max3_f32 v85, v18, v19, v20
	v_max3_f32 v84, v84, v5, v6
	v_max3_f32 v85, v85, v21, v22
	v_max3_f32 v84, v84, v7, v8
	v_max3_f32 v85, v85, v23, v24
	v_max3_f32 v84, v84, v9, v10
	v_max3_f32 v85, v85, v25, v26
	v_max3_f32 v84, v84, v11, v12
	v_max3_f32 v85, v85, v27, v28
	v_max3_f32 v84, v84, v13, v14
	v_max3_f32 v85, v85, v29, v30
	v_max3_f32 v84, v84, v15, v16
	v_max3_f32 v85, v85, v31, v32
	v_max3_f32 v84, v84, v17, v33
	v_max_f32_e32 v84, v84, v85
	v_cmp_lt_f32_e32 vcc, s11, v84
	s_cbranch_vccnz .Lp1_rare_d1a

.LBB4_11:
	s_and_b32 s14, s15, 1
	global_load_dwordx4 v[112:115], v128, s[8:9]
	global_load_dwordx4 v[116:119], v204, s[8:9]
	global_load_dwordx4 v[120:123], v128, s[0:1]
	global_load_dwordx4 v[124:127], v204, s[0:1]
	s_add_i32 s15, s15, 1
	s_mul_i32 s18, s14, 0x2400
	v_add_u32_e32 v202, s18, v167
	ds_read_b128 v[80:83], v202
	ds_read_b128 v[190:193], v202 offset:32
	ds_read_b128 v[194:197], v202 offset:4608
	ds_read_b128 v[198:201], v202 offset:4640
	s_waitcnt lgkmcnt(3)
	v_mfma_f32_32x32x16_f16 v[64:79], v[108:111], v[80:83], v[48:63]
	s_waitcnt lgkmcnt(1)
	v_mfma_f32_32x32x16_f16 v[80:95], v[108:111], v[194:197], v[48:63]
	v_mfma_f32_32x32x16_f16 v[64:79], v[104:107], v[190:193], v[64:79]
	ds_read_b128 v[190:193], v202 offset:64
	ds_read_b128 v[194:197], v202 offset:96
	s_waitcnt lgkmcnt(2)
	v_mfma_f32_32x32x16_f16 v[80:95], v[104:107], v[198:201], v[80:95]
	s_waitcnt lgkmcnt(1)
	v_mfma_f32_32x32x16_f16 v[64:79], v[100:103], v[190:193], v[64:79]
	ds_read_b128 v[190:193], v202 offset:4672
	ds_read_b128 v[198:201], v202 offset:4704
	s_waitcnt lgkmcnt(1)
	v_mfma_f32_32x32x16_f16 v[80:95], v[100:103], v[190:193], v[80:95]
	v_mfma_f32_32x32x16_f16 v[64:79], v[96:99], v[194:197], v[64:79]
	s_waitcnt lgkmcnt(0)
	v_mfma_f32_32x32x16_f16 v[80:95], v[96:99], v[198:201], v[80:95]
	s_setprio 2
	s_nop 8
	v_exp_f32_e32 v192, v64
	s_nop 0
	v_exp_f32_e32 v80, v80
	v_exp_f32_e32 v193, v65
	v_exp_f32_e32 v81, v81
	v_mul_f32_e32 v64, v192, v183
	v_exp_f32_e32 v66, v66
	global_store_dword v132, v64, s[42:43] offset:-128
	v_mul_f32_e32 v64, v80, v183
	v_exp_f32_e32 v82, v82
	global_store_dword v132, v64, s[42:43]
	v_mul_f32_e32 v190, v193, v182
	v_exp_f32_e32 v67, v67
	global_store_dword v136, v190, s[42:43] offset:-128
	v_mul_f32_e32 v190, v81, v182
	v_exp_f32_e32 v83, v83
	global_store_dword v136, v190, s[42:43]
	v_mul_f32_e32 v190, v66, v181
	global_store_dword v140, v190, s[42:43] offset:-128
	v_mul_f32_e32 v190, v82, v181
	global_store_dword v140, v190, s[42:43]
	v_mul_f32_e32 v190, v67, v180
	global_store_dword v144, v190, s[42:43] offset:-128
	v_mul_f32_e32 v190, v83, v180
	global_store_dword v144, v190, s[42:43]
	v_exp_f32_e32 v190, v68
	v_cvt_pk_f16_f32 v65, v66, v67
	v_cvt_pk_f16_f32 v67, v82, v83
	v_exp_f32_e32 v82, v84
	v_cvt_pk_f16_f32 v66, v80, v81
	v_mul_f32_e32 v68, v190, v179
	global_store_dword v148, v68, s[42:43] offset:-128
	v_exp_f32_e32 v83, v69
	v_mul_f32_e32 v68, v82, v179
	global_store_dword v148, v68, s[42:43]
	v_exp_f32_e32 v80, v85
	v_mul_f32_e32 v81, v83, v178
	global_store_dword v152, v81, s[42:43] offset:-128
	v_exp_f32_e32 v70, v70
	v_mul_f32_e32 v81, v80, v178
	global_store_dword v152, v81, s[42:43]
	v_exp_f32_e32 v81, v86
	v_mul_f32_e32 v84, v70, v177
	global_store_dword v156, v84, s[42:43] offset:-128
	v_exp_f32_e32 v71, v71
	v_mul_f32_e32 v84, v81, v177
	global_store_dword v156, v84, s[42:43]
	v_exp_f32_e32 v84, v87
	v_mul_f32_e32 v85, v71, v176
	global_store_dword v160, v85, s[42:43] offset:-128
	v_mul_f32_e32 v85, v84, v176
	v_cvt_pk_f16_f32 v64, v192, v193
	global_store_dword v160, v85, s[42:43]
	v_cvt_pk_f16_f32 v69, v70, v71
	v_cvt_pk_f16_f32 v68, v190, v83
	v_exp_f32_e32 v72, v72
	v_cvt_pk_f16_f32 v71, v81, v84
	v_cvt_pk_f16_f32 v70, v82, v80
	ds_write2_b64 v187, v[64:65], v[68:69] offset1:2
	ds_write2_b64 v131, v[66:67], v[70:71] offset0:32 offset1:34
	v_exp_f32_e32 v66, v88
	v_mul_f32_e32 v67, v72, v175
	global_store_dword v162, v67, s[42:43]
	v_exp_f32_e32 v67, v73
	v_mul_f32_e32 v68, v66, v175
	global_store_dword v162, v68, s[42:43] offset:128
	v_exp_f32_e32 v68, v89
	v_mul_f32_e32 v69, v67, v174
	global_store_dword v158, v69, s[42:43]
	v_exp_f32_e32 v69, v74
	v_mul_f32_e32 v70, v68, v174
	global_store_dword v158, v70, s[42:43] offset:128
	v_exp_f32_e32 v70, v90
	v_mul_f32_e32 v71, v69, v173
	global_store_dword v154, v71, s[42:43]
	v_exp_f32_e32 v71, v75
	v_mul_f32_e32 v73, v70, v173
	global_store_dword v154, v73, s[42:43] offset:128
	v_exp_f32_e32 v73, v91
	v_mul_f32_e32 v74, v71, v172
	global_store_dword v150, v74, s[42:43]
	v_mul_f32_e32 v74, v73, v172
	global_store_dword v150, v74, s[42:43] offset:128
	v_cvt_pk_f16_f32 v65, v69, v71
	v_exp_f32_e32 v71, v76
	v_cvt_pk_f16_f32 v64, v72, v67
	v_cvt_pk_f16_f32 v67, v70, v73
	v_exp_f32_e32 v70, v92
	v_cvt_pk_f16_f32 v66, v66, v68
	v_mul_f32_e32 v72, v71, v171
	global_store_dword v146, v72, s[42:43]
	v_exp_f32_e32 v72, v77
	v_mul_f32_e32 v73, v70, v171
	global_store_dword v146, v73, s[42:43] offset:128
	v_exp_f32_e32 v73, v93
	v_mul_f32_e32 v74, v72, v170
	global_store_dword v142, v74, s[42:43]
	v_exp_f32_e32 v74, v78
	v_mul_f32_e32 v75, v73, v170
	global_store_dword v142, v75, s[42:43] offset:128
	v_exp_f32_e32 v75, v94
	v_mul_f32_e32 v76, v74, v169
	global_store_dword v138, v76, s[42:43]
	v_exp_f32_e32 v76, v79
	v_mul_f32_e32 v77, v75, v169
	global_store_dword v138, v77, s[42:43] offset:128
	v_exp_f32_e32 v77, v95
	v_mul_f32_e32 v78, v76, v168
	global_store_dword v134, v78, s[42:43]
	v_mul_f32_e32 v78, v77, v168
	global_store_dword v134, v78, s[42:43] offset:128
	v_cvt_pk_f16_f32 v69, v74, v76
	v_cvt_pk_f16_f32 v68, v71, v72
	v_cvt_pk_f16_f32 v71, v75, v77
	v_cvt_pk_f16_f32 v70, v70, v73
	ds_write2_b64 v187, v[64:65], v[68:69] offset0:4 offset1:6
	ds_write2_b64 v131, v[66:67], v[70:71] offset0:36 offset1:38
	s_setprio 0
	ds_read_b64_tr_b16 v[64:65], v186
	ds_read_b64_tr_b16 v[66:67], v186 offset:288
	s_mul_i32 s18, s14, 0x3000
	v_or_b32_e32 v80, s18, v185
	ds_read_b64_tr_b16 v[68:69], v80
	ds_read_b64_tr_b16 v[70:71], v80 offset:768
	ds_read_b64_tr_b16 v[74:75], v80 offset:832
	ds_read_b64_tr_b16 v[72:73], v80 offset:64
	ds_read_b64_tr_b16 v[76:77], v186 offset:1152
	ds_read_b64_tr_b16 v[78:79], v186 offset:1440
	s_waitcnt lgkmcnt(4)
	v_mfma_f32_32x32x16_f16 v[0:15], v[64:67], v[68:71], v[0:15]
	s_waitcnt lgkmcnt(2)
	v_mfma_f32_32x32x16_f16 v[16:31], v[64:67], v[72:75], v[16:31]
	ds_read_b64_tr_b16 v[64:65], v80 offset:3072
	ds_read_b64_tr_b16 v[66:67], v80 offset:3840
	ds_read_b64_tr_b16 v[70:71], v80 offset:3904
	ds_read_b64_tr_b16 v[68:69], v80 offset:3136
	s_waitcnt lgkmcnt(2)
	v_mfma_f32_32x32x16_f16 v[0:15], v[76:79], v[64:67], v[0:15]
	s_waitcnt lgkmcnt(0)
	v_mfma_f32_32x32x16_f16 v[16:31], v[76:79], v[68:71], v[16:31]
	ds_read_b64_tr_b16 v[64:65], v186 offset:2304
	ds_read_b64_tr_b16 v[66:67], v186 offset:2592
	ds_read_b64_tr_b16 v[68:69], v80 offset:6144
	ds_read_b64_tr_b16 v[70:71], v80 offset:6912
	ds_read_b64_tr_b16 v[74:75], v80 offset:6976
	ds_read_b64_tr_b16 v[72:73], v80 offset:6208
	ds_read_b64_tr_b16 v[76:77], v186 offset:3456
	ds_read_b64_tr_b16 v[78:79], v186 offset:3744
	s_waitcnt lgkmcnt(4)
	v_mfma_f32_32x32x16_f16 v[0:15], v[64:67], v[68:71], v[0:15]
	s_waitcnt lgkmcnt(2)
	v_mfma_f32_32x32x16_f16 v[16:31], v[64:67], v[72:75], v[16:31]
	ds_read_b64_tr_b16 v[64:65], v80 offset:9216
	ds_read_b64_tr_b16 v[66:67], v80 offset:9984
	ds_read_b64_tr_b16 v[70:71], v80 offset:10048
	ds_read_b64_tr_b16 v[68:69], v80 offset:9280
	s_waitcnt lgkmcnt(2)
	v_mfma_f32_32x32x16_f16 v[0:15], v[76:79], v[64:67], v[0:15]
	s_waitcnt lgkmcnt(0)
	v_mfma_f32_32x32x16_f16 v[16:31], v[76:79], v[68:71], v[16:31]
	s_xor_b32 s14, s14, 1
	s_mul_i32 s18, s14, 0x3000
	s_mulk_i32 s14, 0x2400
	s_addk_i32 s14, 0x6000
	s_add_u32 s10, s10, 0x100
	s_addc_u32 s11, s11, 0
	s_add_u32 s42, s42, 0x100
	s_addc_u32 s43, s43, 0
	s_add_u32 s8, s8, 0x2000
	s_addc_u32 s9, s9, 0
	s_add_u32 s0, s0, 0x2000
	s_addc_u32 s1, s1, 0
	v_lshl_add_u32 v67, v166, 1, s14
	s_cmpk_eq_i32 s10, 0x1f00
	v_lshl_add_u32 v64, v189, 1, s18
	v_lshl_add_u32 v65, v188, 1, s18
	v_lshl_add_u32 v66, v165, 1, s14
	s_waitcnt vmcnt(32)
	ds_write_b128 v67, v[112:115]
	ds_write_b128 v66, v[116:119]
	ds_write_b128 v65, v[120:123]
	ds_write_b128 v64, v[124:127]
	s_waitcnt lgkmcnt(0)
	s_barrier
	s_cbranch_scc0 .LBB4_11
	s_lshl_b64 s[0:1], s[16:17], 13
	s_add_u32 s0, s4, s0
	s_addc_u32 s1, s5, s1
	v_xor_b32_e32 v52, 0x80000000, v34
	v_xor_b32_e32 v51, 0x80000000, v35
	v_xor_b32_e32 v50, 0x80000000, v32
	v_xor_b32_e32 v49, 0x80000000, v33
	ds_read_b128 v[32:35], v167 offset:9216
	v_xor_b32_e32 v59, 0x80000000, v43
	v_xor_b32_e32 v58, 0x80000000, v40
	v_xor_b32_e32 v57, 0x80000000, v41
	v_xor_b32_e32 v56, 0x80000000, v38
	v_xor_b32_e32 v55, 0x80000000, v39
	v_xor_b32_e32 v54, 0x80000000, v36
	v_xor_b32_e32 v53, 0x80000000, v37
	v_xor_b32_e32 v48, 0x80000000, v46
	v_xor_b32_e32 v47, 0x80000000, v47
	v_xor_b32_e32 v46, 0x80000000, v42
	v_xor_b32_e32 v45, 0x80000000, v45
	v_xor_b32_e32 v44, 0x80000000, v44
	ds_read_b128 v[36:39], v167 offset:9248
	s_add_u32 s0, s0, 0x1f00
	s_waitcnt lgkmcnt(1)
	v_mfma_f32_32x32x16_f16 v[60:75], v[108:111], v[32:35], v[44:59]
	ds_read_b128 v[32:35], v167 offset:13824
	ds_read_b128 v[40:43], v167 offset:13856
	s_addc_u32 s1, s1, 0
	s_waitcnt lgkmcnt(1)
	v_mfma_f32_32x32x16_f16 v[44:59], v[108:111], v[32:35], v[44:59]
	v_mfma_f32_32x32x16_f16 v[60:75], v[104:107], v[36:39], v[60:75]
	ds_read_b128 v[32:35], v167 offset:9280
	ds_read_b128 v[36:39], v167 offset:9312
	s_waitcnt lgkmcnt(2)
	v_mfma_f32_32x32x16_f16 v[44:59], v[104:107], v[40:43], v[44:59]
	s_waitcnt lgkmcnt(1)
	v_mfma_f32_32x32x16_f16 v[60:75], v[100:103], v[32:35], v[60:75]
	ds_read_b128 v[32:35], v167 offset:13888
	ds_read_b128 v[40:43], v167 offset:13920
	s_waitcnt lgkmcnt(1)
	v_mfma_f32_32x32x16_f16 v[44:59], v[100:103], v[32:35], v[44:59]
	v_mfma_f32_32x32x16_f16 v[60:75], v[96:99], v[36:39], v[60:75]
	s_waitcnt lgkmcnt(0)
	v_mfma_f32_32x32x16_f16 v[44:59], v[96:99], v[40:43], v[44:59]
	s_setprio 2
	s_nop 8
	v_exp_f32_e32 v32, v60
	s_nop 0
	v_exp_f32_e32 v34, v44
	v_exp_f32_e32 v35, v61
	v_or_b32_e32 v37, 0x2000, v130
	v_mul_f32_e32 v33, v32, v183
	v_mul_f32_e32 v36, v34, v183
	global_store_dword v130, v33, s[0:1]
	global_store_dword v130, v36, s[0:1] offset:128
	v_exp_f32_e32 v36, v45
	v_mul_f32_e32 v33, v35, v182
	global_store_dword v37, v33, s[0:1]
	v_exp_f32_e32 v33, v62
	v_mul_f32_e32 v38, v36, v182
	global_store_dword v37, v38, s[0:1] offset:128
	v_exp_f32_e32 v37, v46
	v_mul_f32_e32 v38, v33, v181
	v_or_b32_e32 v39, 0x4000, v130
	global_store_dword v39, v38, s[0:1]
	v_exp_f32_e32 v38, v63
	v_mul_f32_e32 v40, v37, v181
	global_store_dword v39, v40, s[0:1] offset:128
	v_exp_f32_e32 v39, v47
	v_mul_f32_e32 v40, v38, v180
	v_cvt_pk_f16_f32 v33, v33, v38
	v_exp_f32_e32 v38, v64
	v_or_b32_e32 v41, 0x6000, v130
	global_store_dword v41, v40, s[0:1]
	v_mul_f32_e32 v40, v39, v180
	global_store_dword v41, v40, s[0:1] offset:128
	v_cvt_pk_f16_f32 v32, v32, v35
	v_cvt_pk_f16_f32 v35, v37, v39
	v_cvt_pk_f16_f32 v34, v34, v36
	v_exp_f32_e32 v40, v48
	v_mul_f32_e32 v36, v38, v179
	v_or_b32_e32 v37, 0x10000, v130
	global_store_dword v37, v36, s[0:1]
	v_exp_f32_e32 v36, v65
	v_exp_f32_e32 v41, v49
	v_mul_f32_e32 v39, v40, v179
	global_store_dword v37, v39, s[0:1] offset:128
	v_mul_f32_e32 v37, v36, v178
	v_or_b32_e32 v39, 0x12000, v130
	global_store_dword v39, v37, s[0:1]
	v_exp_f32_e32 v37, v66
	v_mul_f32_e32 v42, v41, v178
	global_store_dword v39, v42, s[0:1] offset:128
	v_exp_f32_e32 v39, v50
	v_mul_f32_e32 v42, v37, v177
	v_or_b32_e32 v43, 0x14000, v130
	global_store_dword v43, v42, s[0:1]
	v_exp_f32_e32 v42, v67
	v_mul_f32_e32 v44, v39, v177
	global_store_dword v43, v44, s[0:1] offset:128
	v_exp_f32_e32 v43, v51
	v_cvt_pk_f16_f32 v37, v37, v42
	v_cvt_pk_f16_f32 v36, v38, v36
	v_cvt_pk_f16_f32 v38, v40, v41
	v_cvt_pk_f16_f32 v39, v39, v43
	ds_write2_b64 v187, v[32:33], v[36:37] offset1:2
	v_exp_f32_e32 v32, v68
	v_add_u32_e32 v40, 0x800, v187
	ds_write2_b64 v40, v[34:35], v[38:39] offset0:32 offset1:34
	v_exp_f32_e32 v34, v52
	v_exp_f32_e32 v36, v69
	v_exp_f32_e32 v37, v53
	v_mul_f32_e32 v33, v32, v175
	v_or_b32_e32 v35, 0x20000, v130
	global_store_dword v35, v33, s[0:1]
	v_mul_f32_e32 v33, v34, v175
	global_store_dword v35, v33, s[0:1] offset:128
	v_mul_f32_e32 v33, v36, v174
	v_or_b32_e32 v35, 0x22000, v130
	global_store_dword v35, v33, s[0:1]
	v_exp_f32_e32 v33, v70
	v_mul_f32_e32 v38, v37, v174
	global_store_dword v35, v38, s[0:1] offset:128
	v_exp_f32_e32 v35, v54
	v_mul_f32_e32 v38, v33, v173
	v_or_b32_e32 v39, 0x24000, v130
	global_store_dword v39, v38, s[0:1]
	v_exp_f32_e32 v38, v71
	v_mul_f32_e32 v41, v35, v173
	global_store_dword v39, v41, s[0:1] offset:128
	v_exp_f32_e32 v39, v55
	v_mul_f32_e32 v44, v42, v176
	v_mul_f32_e32 v41, v38, v172
	v_or_b32_e32 v42, 0x26000, v130
	v_cvt_pk_f16_f32 v32, v32, v36
	v_exp_f32_e32 v36, v72
	global_store_dword v42, v41, s[0:1]
	v_mul_f32_e32 v41, v39, v172
	v_cvt_pk_f16_f32 v33, v33, v38
	v_exp_f32_e32 v38, v56
	global_store_dword v42, v41, s[0:1] offset:128
	v_exp_f32_e32 v41, v73
	v_exp_f32_e32 v42, v57
	v_cvt_pk_f16_f32 v35, v35, v39
	v_cvt_pk_f16_f32 v34, v34, v37
	v_mul_f32_e32 v37, v36, v171
	v_or_b32_e32 v39, 0x30000, v130
	global_store_dword v39, v37, s[0:1]
	v_mul_f32_e32 v37, v38, v171
	v_or_b32_e32 v45, 0x16000, v130
	global_store_dword v39, v37, s[0:1] offset:128
	v_mul_f32_e32 v37, v41, v170
	v_or_b32_e32 v39, 0x32000, v130
	global_store_dword v45, v44, s[0:1]
	v_mul_f32_e32 v44, v43, v176
	global_store_dword v39, v37, s[0:1]
	v_exp_f32_e32 v37, v74
	v_mul_f32_e32 v43, v42, v170
	global_store_dword v39, v43, s[0:1] offset:128
	v_exp_f32_e32 v39, v58
	global_store_dword v45, v44, s[0:1] offset:128
	v_mul_f32_e32 v43, v37, v169
	v_or_b32_e32 v44, 0x34000, v130
	global_store_dword v44, v43, s[0:1]
	v_exp_f32_e32 v43, v75
	v_mul_f32_e32 v45, v39, v169
	global_store_dword v44, v45, s[0:1] offset:128
	v_exp_f32_e32 v44, v59
	v_mul_f32_e32 v45, v43, v168
	v_or_b32_e32 v46, 0x36000, v130
	global_store_dword v46, v45, s[0:1]
	v_mul_f32_e32 v45, v44, v168
	v_cvt_pk_f16_f32 v37, v37, v43
	v_cvt_pk_f16_f32 v36, v36, v41
	global_store_dword v46, v45, s[0:1] offset:128
	v_cvt_pk_f16_f32 v39, v39, v44
	v_cvt_pk_f16_f32 v38, v38, v42
	ds_write2_b64 v187, v[32:33], v[36:37] offset0:4 offset1:6
	ds_write2_b64 v40, v[34:35], v[38:39] offset0:36 offset1:38
	s_setprio 0
	ds_read_b64_tr_b16 v[32:33], v186
	ds_read_b64_tr_b16 v[34:35], v186 offset:288
	ds_read_b64_tr_b16 v[36:37], v185 offset:12288
	ds_read_b64_tr_b16 v[38:39], v185 offset:13056
	ds_read_b64_tr_b16 v[42:43], v185 offset:13120
	ds_read_b64_tr_b16 v[40:41], v185 offset:12352
	ds_read_b64_tr_b16 v[44:45], v186 offset:1152
	ds_read_b64_tr_b16 v[46:47], v186 offset:1440
	s_waitcnt lgkmcnt(4)
	v_mfma_f32_32x32x16_f16 v[0:15], v[32:35], v[36:39], v[0:15]
	s_waitcnt lgkmcnt(2)
	v_mfma_f32_32x32x16_f16 v[16:31], v[32:35], v[40:43], v[16:31]
	ds_read_b64_tr_b16 v[32:33], v185 offset:15360
	ds_read_b64_tr_b16 v[34:35], v185 offset:16128
	ds_read_b64_tr_b16 v[38:39], v185 offset:16192
	ds_read_b64_tr_b16 v[36:37], v185 offset:15424
	s_waitcnt lgkmcnt(2)
	v_mfma_f32_32x32x16_f16 v[0:15], v[44:47], v[32:35], v[0:15]
	s_waitcnt lgkmcnt(0)
	v_mfma_f32_32x32x16_f16 v[16:31], v[44:47], v[36:39], v[16:31]
	ds_read_b64_tr_b16 v[32:33], v186 offset:2304
	ds_read_b64_tr_b16 v[34:35], v186 offset:2592
	ds_read_b64_tr_b16 v[36:37], v185 offset:18432
	ds_read_b64_tr_b16 v[38:39], v185 offset:19200
	ds_read_b64_tr_b16 v[42:43], v185 offset:19264
	ds_read_b64_tr_b16 v[40:41], v185 offset:18496
	ds_read_b64_tr_b16 v[44:45], v186 offset:3456
	ds_read_b64_tr_b16 v[46:47], v186 offset:3744
	s_waitcnt lgkmcnt(4)
	v_mfma_f32_32x32x16_f16 v[0:15], v[32:35], v[36:39], v[0:15]
	s_waitcnt lgkmcnt(2)
	v_mfma_f32_32x32x16_f16 v[16:31], v[32:35], v[40:43], v[16:31]
	ds_read_b64_tr_b16 v[32:33], v185 offset:21504
	ds_read_b64_tr_b16 v[34:35], v185 offset:22272
	ds_read_b64_tr_b16 v[38:39], v185 offset:22336
	ds_read_b64_tr_b16 v[36:37], v185 offset:21568
	s_waitcnt lgkmcnt(2)
	v_mfma_f32_32x32x16_f16 v[0:15], v[44:47], v[32:35], v[0:15]
	s_waitcnt lgkmcnt(0)
	v_mfma_f32_32x32x16_f16 v[16:31], v[44:47], v[36:39], v[16:31]
	s_lshl_b32 s0, s2, 3
	s_and_b32 s0, s0, 0x7ffff800
	s_add_i32 s3, s3, s0
	s_lshl_b32 s0, s12, 7
	s_and_b32 s0, s0, 0x780
	s_add_u32 s0, s6, s0
	v_mov_b32_e32 v35, 0
	v_or_b32_e32 v32, s3, v184
	s_addc_u32 s1, s7, 0
	v_lshlrev_b32_e32 v34, 1, v164
	v_mov_b32_e32 v33, v35
	v_lshl_add_u64 v[36:37], s[0:1], 0, v[34:35]
	v_lshlrev_b64 v[38:39], 11, v[32:33]
	v_fma_mixlo_f16 v0, v0, v183, 0
	v_lshl_add_u64 v[38:39], v[36:37], 0, v[38:39]
	s_waitcnt vmcnt(63) expcnt(7) lgkmcnt(15)
	s_barrier
	global_store_short v[38:39], v0, off
	v_fma_mixlo_f16 v0, v16, v183, 0
	v_or_b32_e32 v34, 1, v32
	global_store_short v[38:39], v0, off offset:64
	v_lshlrev_b64 v[38:39], 11, v[34:35]
	v_fma_mixlo_f16 v16, v1, v182, 0
	v_lshl_add_u64 v[0:1], v[36:37], 0, v[38:39]
	global_store_short v[0:1], v16, off
	v_fma_mixlo_f16 v16, v17, v182, 0
	v_or_b32_e32 v34, 2, v32
	global_store_short v[0:1], v16, off offset:64
	v_lshlrev_b64 v[0:1], 11, v[34:35]
	v_fma_mixlo_f16 v2, v2, v181, 0
	v_lshl_add_u64 v[0:1], v[36:37], 0, v[0:1]
	global_store_short v[0:1], v2, off
	v_fma_mixlo_f16 v2, v18, v181, 0
	v_or_b32_e32 v34, 3, v32
	global_store_short v[0:1], v2, off offset:64
	v_lshlrev_b64 v[0:1], 11, v[34:35]
	v_fma_mixlo_f16 v2, v3, v180, 0
	v_lshl_add_u64 v[0:1], v[36:37], 0, v[0:1]
	global_store_short v[0:1], v2, off
	v_fma_mixlo_f16 v2, v19, v180, 0
	v_or_b32_e32 v34, 8, v32
	global_store_short v[0:1], v2, off offset:64
	v_lshlrev_b64 v[0:1], 11, v[34:35]
	v_fma_mixlo_f16 v2, v4, v179, 0
	v_lshl_add_u64 v[0:1], v[36:37], 0, v[0:1]
	global_store_short v[0:1], v2, off
	v_fma_mixlo_f16 v2, v20, v179, 0
	v_or_b32_e32 v34, 9, v32
	global_store_short v[0:1], v2, off offset:64
	v_lshlrev_b64 v[0:1], 11, v[34:35]
	v_fma_mixlo_f16 v2, v5, v178, 0
	v_lshl_add_u64 v[0:1], v[36:37], 0, v[0:1]
	global_store_short v[0:1], v2, off
	v_fma_mixlo_f16 v2, v21, v178, 0
	v_or_b32_e32 v34, 10, v32
	global_store_short v[0:1], v2, off offset:64
	v_lshlrev_b64 v[0:1], 11, v[34:35]
	v_fma_mixlo_f16 v2, v6, v177, 0
	v_lshl_add_u64 v[0:1], v[36:37], 0, v[0:1]
	global_store_short v[0:1], v2, off
	v_fma_mixlo_f16 v2, v22, v177, 0
	v_or_b32_e32 v34, 11, v32
	global_store_short v[0:1], v2, off offset:64
	v_lshlrev_b64 v[0:1], 11, v[34:35]
	v_fma_mixlo_f16 v2, v7, v176, 0
	v_lshl_add_u64 v[0:1], v[36:37], 0, v[0:1]
	global_store_short v[0:1], v2, off
	v_fma_mixlo_f16 v2, v23, v176, 0
	v_or_b32_e32 v34, 16, v32
	global_store_short v[0:1], v2, off offset:64
	v_lshlrev_b64 v[0:1], 11, v[34:35]
	v_fma_mixlo_f16 v2, v8, v175, 0
	v_lshl_add_u64 v[0:1], v[36:37], 0, v[0:1]
	global_store_short v[0:1], v2, off
	v_fma_mixlo_f16 v2, v24, v175, 0
	v_or_b32_e32 v34, 17, v32
	global_store_short v[0:1], v2, off offset:64
	v_lshlrev_b64 v[0:1], 11, v[34:35]
	v_fma_mixlo_f16 v2, v9, v174, 0
	v_lshl_add_u64 v[0:1], v[36:37], 0, v[0:1]
	global_store_short v[0:1], v2, off
	v_fma_mixlo_f16 v2, v25, v174, 0
	v_or_b32_e32 v34, 18, v32
	global_store_short v[0:1], v2, off offset:64
	v_lshlrev_b64 v[0:1], 11, v[34:35]
	v_fma_mixlo_f16 v2, v10, v173, 0
	v_lshl_add_u64 v[0:1], v[36:37], 0, v[0:1]
	global_store_short v[0:1], v2, off
	v_fma_mixlo_f16 v2, v26, v173, 0
	v_or_b32_e32 v34, 19, v32
	global_store_short v[0:1], v2, off offset:64
	v_lshlrev_b64 v[0:1], 11, v[34:35]
	v_fma_mixlo_f16 v2, v11, v172, 0
	v_lshl_add_u64 v[0:1], v[36:37], 0, v[0:1]
	global_store_short v[0:1], v2, off
	v_fma_mixlo_f16 v2, v27, v172, 0
	v_or_b32_e32 v34, 24, v32
	global_store_short v[0:1], v2, off offset:64
	v_lshlrev_b64 v[0:1], 11, v[34:35]
	v_fma_mixlo_f16 v2, v12, v171, 0
	v_lshl_add_u64 v[0:1], v[36:37], 0, v[0:1]
	global_store_short v[0:1], v2, off
	v_fma_mixlo_f16 v2, v28, v171, 0
	v_or_b32_e32 v34, 25, v32
	global_store_short v[0:1], v2, off offset:64
	v_lshlrev_b64 v[0:1], 11, v[34:35]
	v_fma_mixlo_f16 v2, v13, v170, 0
	v_lshl_add_u64 v[0:1], v[36:37], 0, v[0:1]
	global_store_short v[0:1], v2, off
	v_fma_mixlo_f16 v2, v29, v170, 0
	v_or_b32_e32 v34, 26, v32
	global_store_short v[0:1], v2, off offset:64
	v_lshlrev_b64 v[0:1], 11, v[34:35]
	v_fma_mixlo_f16 v2, v14, v169, 0
	v_lshl_add_u64 v[0:1], v[36:37], 0, v[0:1]
	global_store_short v[0:1], v2, off
	v_fma_mixlo_f16 v2, v30, v169, 0
	v_or_b32_e32 v34, 27, v32
	global_store_short v[0:1], v2, off offset:64
	v_lshlrev_b64 v[0:1], 11, v[34:35]
	v_fma_mixlo_f16 v2, v15, v168, 0
	v_lshl_add_u64 v[0:1], v[36:37], 0, v[0:1]
	global_store_short v[0:1], v2, off
	v_fma_mixlo_f16 v2, v31, v168, 0
	global_store_short v[0:1], v2, off offset:64
	s_endpgm
	.p2alignl 8, 3212836864
